# v46: v34 with the nt hint removed from the attention part stores (cache-policy experiment)
# baseline (speedup 1.0000x reference)
; #define SBAR() __builtin_amdgcn_sched_barrier(0)
; __device__ __forceinline__ int crow(int r, int hi) { return (r & 3) + 8 * (r >> 2) + 4 * hi; }
; #define SEAM_K0() do { VMWN(NQL); if constexpr (F32) { SWRITE_KF(0); SBAR(); SLOAD_F((const float*)nxt.V, kbn); } else { SWRITE_HK(0); } SBAR(); } while (0)
; template <class TIn, class TOut>
; __device__ __forceinline__ void causal_swa_block(const BlockRef<TIn, TOut>& cur, const BlockRef<TIn, TOut>& nxt, int skv, int W, char* lds, Seam<TIn>& S) {
;     ...
;     SBAR(); SEAM_K0();
;     {
;         bf16* Pw = cur.PO + (size_t)(wid * QBLK) * 128;
; #pragma unroll
;         for (int r = 0; r < 16; ++r) { const int orow = crow(r, hi);
; #pragma unroll
;             for (int d0 = 0; d0 < 4; ++d0) { const float v = o[d0][r]; const float vn = __shfl_xor(v, 1);
;                 if ((r32 & 1) == 0) __builtin_nontemporal_store(cvtpk(v, vn), (unsigned*)(Pw + (size_t)orow * 128 + d0 * 32 + r32)); } }
.LBB0_749:
	s_waitcnt vmcnt(8)
	s_waitcnt vmcnt(9)
	ds_write_b128 v224, v[106:109] offset:32768
	s_waitcnt vmcnt(8)
	ds_write_b128 v224, v[110:113] offset:40960
	s_lshl_b64 s[0:1], s[10:11], 8
	v_mov_b32_dpp v68, v50 quad_perm:[1,0,3,2] row_mask:0xf bank_mask:0xf
	s_add_u32 s0, s34, s0
	s_addc_u32 s1, s35, s1
	v_lshlrev_b32_e32 v66, 1, v194
	v_mov_b32_e32 v67, v197
	v_lshl_add_u64 v[66:67], s[0:1], 0, v[66:67]
	v_lshl_add_u64 v[66:67], v[66:67], 0, v[200:201]
	s_and_saveexec_b64 s[0:1], s[4:5]
	s_cbranch_execz .LBB0_751
	s_waitcnt lgkmcnt(0)
	v_cvt_pk_bf16_f32 v50, v50, v68
	global_store_dword v[66:67], v50, off
.LBB0_751:
	s_or_b64 exec, exec, s[0:1]
	v_mov_b32_dpp v50, v34 quad_perm:[1,0,3,2] row_mask:0xf bank_mask:0xf
	s_and_saveexec_b64 s[0:1], s[4:5]
	s_cbranch_execz .LBB0_753
	s_waitcnt lgkmcnt(0)
	v_cvt_pk_bf16_f32 v34, v34, v50
	global_store_dword v[66:67], v34, off offset:64
.LBB0_753:
	s_or_b64 exec, exec, s[0:1]
	v_mov_b32_dpp v34, v18 quad_perm:[1,0,3,2] row_mask:0xf bank_mask:0xf
	s_and_saveexec_b64 s[0:1], s[4:5]
	s_cbranch_execz .LBB0_755
	s_waitcnt lgkmcnt(0)
	v_cvt_pk_bf16_f32 v18, v18, v34
	global_store_dword v[66:67], v18, off offset:128
.LBB0_755:
	s_or_b64 exec, exec, s[0:1]
	v_mov_b32_dpp v18, v2 quad_perm:[1,0,3,2] row_mask:0xf bank_mask:0xf
	s_and_saveexec_b64 s[0:1], s[4:5]
	s_cbranch_execz .LBB0_757
	s_waitcnt lgkmcnt(0)
	v_cvt_pk_bf16_f32 v2, v2, v18
	global_store_dword v[66:67], v2, off offset:192
.LBB0_757:
	s_or_b64 exec, exec, s[0:1]
	v_mov_b32_dpp v2, v51 quad_perm:[1,0,3,2] row_mask:0xf bank_mask:0xf
	s_and_saveexec_b64 s[0:1], s[4:5]
	s_cbranch_execz .LBB0_759
	s_waitcnt lgkmcnt(0)
	v_cvt_pk_bf16_f32 v2, v51, v2
	global_store_dword v[66:67], v2, off offset:256
.LBB0_759:
	s_or_b64 exec, exec, s[0:1]
	s_waitcnt lgkmcnt(0)
	v_mov_b32_dpp v2, v35 quad_perm:[1,0,3,2] row_mask:0xf bank_mask:0xf
	s_and_saveexec_b64 s[0:1], s[4:5]
	s_cbranch_execz .LBB0_761
	s_waitcnt lgkmcnt(0)
	v_cvt_pk_bf16_f32 v2, v35, v2
	global_store_dword v[66:67], v2, off offset:320
.LBB0_761:
	s_or_b64 exec, exec, s[0:1]
	s_waitcnt lgkmcnt(0)
	v_mov_b32_dpp v2, v19 quad_perm:[1,0,3,2] row_mask:0xf bank_mask:0xf
	s_and_saveexec_b64 s[0:1], s[4:5]
	s_cbranch_execz .LBB0_763
	s_waitcnt lgkmcnt(0)
	v_cvt_pk_bf16_f32 v2, v19, v2
	global_store_dword v[66:67], v2, off offset:384
.LBB0_763:
	s_or_b64 exec, exec, s[0:1]
	s_waitcnt lgkmcnt(0)
	v_mov_b32_dpp v2, v3 quad_perm:[1,0,3,2] row_mask:0xf bank_mask:0xf
	s_and_saveexec_b64 s[0:1], s[4:5]
	s_cbranch_execz .LBB0_765
	s_waitcnt lgkmcnt(0)
	v_cvt_pk_bf16_f32 v2, v3, v2
	global_store_dword v[66:67], v2, off offset:448
.LBB0_765:
	s_or_b64 exec, exec, s[0:1]
	s_waitcnt lgkmcnt(0)
	v_mov_b32_dpp v2, v52 quad_perm:[1,0,3,2] row_mask:0xf bank_mask:0xf
	s_and_saveexec_b64 s[0:1], s[4:5]
	s_cbranch_execz .LBB0_767
	s_waitcnt lgkmcnt(0)
	v_cvt_pk_bf16_f32 v2, v52, v2
	global_store_dword v[66:67], v2, off offset:512
.LBB0_767:
	s_or_b64 exec, exec, s[0:1]
	s_waitcnt lgkmcnt(0)
	v_mov_b32_dpp v2, v36 quad_perm:[1,0,3,2] row_mask:0xf bank_mask:0xf
	s_and_saveexec_b64 s[0:1], s[4:5]
	s_cbranch_execz .LBB0_769
	s_waitcnt lgkmcnt(0)
	v_cvt_pk_bf16_f32 v2, v36, v2
	global_store_dword v[66:67], v2, off offset:576
.LBB0_769:
	s_or_b64 exec, exec, s[0:1]
	s_waitcnt lgkmcnt(0)
	v_mov_b32_dpp v2, v20 quad_perm:[1,0,3,2] row_mask:0xf bank_mask:0xf
	s_and_saveexec_b64 s[0:1], s[4:5]
	s_cbranch_execz .LBB0_771
	s_waitcnt lgkmcnt(0)
	v_cvt_pk_bf16_f32 v2, v20, v2
	global_store_dword v[66:67], v2, off offset:640
.LBB0_771:
	s_or_b64 exec, exec, s[0:1]
	s_waitcnt lgkmcnt(0)
	v_mov_b32_dpp v2, v4 quad_perm:[1,0,3,2] row_mask:0xf bank_mask:0xf
	s_and_saveexec_b64 s[0:1], s[4:5]
	s_cbranch_execz .LBB0_773
	s_waitcnt lgkmcnt(0)
	v_cvt_pk_bf16_f32 v2, v4, v2
	global_store_dword v[66:67], v2, off offset:704
.LBB0_773:
	s_or_b64 exec, exec, s[0:1]
	s_waitcnt lgkmcnt(0)
	v_mov_b32_dpp v2, v53 quad_perm:[1,0,3,2] row_mask:0xf bank_mask:0xf
	s_and_saveexec_b64 s[0:1], s[4:5]
	s_cbranch_execz .LBB0_775
	s_waitcnt lgkmcnt(0)
	v_cvt_pk_bf16_f32 v2, v53, v2
	global_store_dword v[66:67], v2, off offset:768
.LBB0_775:
	s_or_b64 exec, exec, s[0:1]
	s_waitcnt lgkmcnt(0)
	v_mov_b32_dpp v2, v37 quad_perm:[1,0,3,2] row_mask:0xf bank_mask:0xf
	s_and_saveexec_b64 s[0:1], s[4:5]
	s_cbranch_execz .LBB0_777
	s_waitcnt lgkmcnt(0)
	v_cvt_pk_bf16_f32 v2, v37, v2
	global_store_dword v[66:67], v2, off offset:832
.LBB0_777:
	s_or_b64 exec, exec, s[0:1]
	s_waitcnt lgkmcnt(0)
	v_mov_b32_dpp v2, v21 quad_perm:[1,0,3,2] row_mask:0xf bank_mask:0xf
	s_and_saveexec_b64 s[0:1], s[4:5]
	s_cbranch_execz .LBB0_779
	s_waitcnt lgkmcnt(0)
	v_cvt_pk_bf16_f32 v2, v21, v2
	global_store_dword v[66:67], v2, off offset:896
.LBB0_779:
	s_or_b64 exec, exec, s[0:1]
	s_waitcnt lgkmcnt(0)
	v_mov_b32_dpp v2, v5 quad_perm:[1,0,3,2] row_mask:0xf bank_mask:0xf
	s_and_saveexec_b64 s[0:1], s[4:5]
	s_cbranch_execz .LBB0_781
	s_waitcnt lgkmcnt(0)
	v_cvt_pk_bf16_f32 v2, v5, v2
	global_store_dword v[66:67], v2, off offset:960
.LBB0_781:
	s_or_b64 exec, exec, s[0:1]
	s_waitcnt lgkmcnt(0)
	v_mov_b32_dpp v2, v54 quad_perm:[1,0,3,2] row_mask:0xf bank_mask:0xf
	s_and_saveexec_b64 s[0:1], s[4:5]
	s_cbranch_execz .LBB0_783
	s_waitcnt lgkmcnt(0)
	v_cvt_pk_bf16_f32 v2, v54, v2
	global_store_dword v[66:67], v2, off offset:2048
.LBB0_783:
	s_or_b64 exec, exec, s[0:1]
	s_waitcnt lgkmcnt(0)
	v_mov_b32_dpp v2, v38 quad_perm:[1,0,3,2] row_mask:0xf bank_mask:0xf
	s_and_saveexec_b64 s[0:1], s[4:5]
	s_cbranch_execz .LBB0_785
	s_waitcnt lgkmcnt(0)
	v_cvt_pk_bf16_f32 v2, v38, v2
	global_store_dword v[66:67], v2, off offset:2112
; __device__ __forceinline__ int crow(int r, int hi) { return (r & 3) + 8 * (r >> 2) + 4 * hi; }
; template <class TIn, class TOut>
; __device__ __forceinline__ void causal_swa_block(const BlockRef<TIn, TOut>& cur, const BlockRef<TIn, TOut>& nxt, int skv, int W, char* lds, Seam<TIn>& S) {
;     ...
;         for (int r = 0; r < 16; ++r) { const int orow = crow(r, hi);
; #pragma unroll
;             for (int d0 = 0; d0 < 4; ++d0) { const float v = o[d0][r]; const float vn = __shfl_xor(v, 1);
;                 if ((r32 & 1) == 0) __builtin_nontemporal_store(cvtpk(v, vn), (unsigned*)(Pw + (size_t)orow * 128 + d0 * 32 + r32)); } }
.LBB0_785:
	s_or_b64 exec, exec, s[0:1]
	s_waitcnt lgkmcnt(0)
	v_mov_b32_dpp v2, v22 quad_perm:[1,0,3,2] row_mask:0xf bank_mask:0xf
	s_and_saveexec_b64 s[0:1], s[4:5]
	s_cbranch_execz .LBB0_787
	s_waitcnt lgkmcnt(0)
	v_cvt_pk_bf16_f32 v2, v22, v2
	global_store_dword v[66:67], v2, off offset:2176
.LBB0_787:
	s_or_b64 exec, exec, s[0:1]
	s_waitcnt lgkmcnt(0)
	v_mov_b32_dpp v2, v6 quad_perm:[1,0,3,2] row_mask:0xf bank_mask:0xf
	s_and_saveexec_b64 s[0:1], s[4:5]
	s_cbranch_execz .LBB0_789
	s_waitcnt lgkmcnt(0)
	v_cvt_pk_bf16_f32 v2, v6, v2
	global_store_dword v[66:67], v2, off offset:2240
.LBB0_789:
	s_or_b64 exec, exec, s[0:1]
	s_waitcnt lgkmcnt(0)
	v_mov_b32_dpp v2, v55 quad_perm:[1,0,3,2] row_mask:0xf bank_mask:0xf
	s_and_saveexec_b64 s[0:1], s[4:5]
	s_cbranch_execz .LBB0_791
	s_waitcnt lgkmcnt(0)
	v_cvt_pk_bf16_f32 v2, v55, v2
	global_store_dword v[66:67], v2, off offset:2304
.LBB0_791:
	s_or_b64 exec, exec, s[0:1]
	s_waitcnt lgkmcnt(0)
	v_mov_b32_dpp v2, v39 quad_perm:[1,0,3,2] row_mask:0xf bank_mask:0xf
	s_and_saveexec_b64 s[0:1], s[4:5]
	s_cbranch_execz .LBB0_793
	s_waitcnt lgkmcnt(0)
	v_cvt_pk_bf16_f32 v2, v39, v2
	global_store_dword v[66:67], v2, off offset:2368
.LBB0_793:
	s_or_b64 exec, exec, s[0:1]
	s_waitcnt lgkmcnt(0)
	v_mov_b32_dpp v2, v23 quad_perm:[1,0,3,2] row_mask:0xf bank_mask:0xf
	s_and_saveexec_b64 s[0:1], s[4:5]
	s_cbranch_execz .LBB0_795
	s_waitcnt lgkmcnt(0)
	v_cvt_pk_bf16_f32 v2, v23, v2
	global_store_dword v[66:67], v2, off offset:2432
.LBB0_795:
	s_or_b64 exec, exec, s[0:1]
	s_waitcnt lgkmcnt(0)
	v_mov_b32_dpp v2, v7 quad_perm:[1,0,3,2] row_mask:0xf bank_mask:0xf
	s_and_saveexec_b64 s[0:1], s[4:5]
	s_cbranch_execz .LBB0_797
	s_waitcnt lgkmcnt(0)
	v_cvt_pk_bf16_f32 v2, v7, v2
	global_store_dword v[66:67], v2, off offset:2496
.LBB0_797:
	s_or_b64 exec, exec, s[0:1]
	s_waitcnt lgkmcnt(0)
	v_mov_b32_dpp v2, v56 quad_perm:[1,0,3,2] row_mask:0xf bank_mask:0xf
	s_and_saveexec_b64 s[0:1], s[4:5]
	s_cbranch_execz .LBB0_799
	s_waitcnt lgkmcnt(0)
	v_cvt_pk_bf16_f32 v2, v56, v2
	global_store_dword v[66:67], v2, off offset:2560
.LBB0_799:
	s_or_b64 exec, exec, s[0:1]
	s_waitcnt lgkmcnt(0)
	v_mov_b32_dpp v2, v40 quad_perm:[1,0,3,2] row_mask:0xf bank_mask:0xf
	s_and_saveexec_b64 s[0:1], s[4:5]
	s_cbranch_execz .LBB0_801
	s_waitcnt lgkmcnt(0)
	v_cvt_pk_bf16_f32 v2, v40, v2
	global_store_dword v[66:67], v2, off offset:2624
.LBB0_801:
	s_or_b64 exec, exec, s[0:1]
	s_waitcnt lgkmcnt(0)
	v_mov_b32_dpp v2, v24 quad_perm:[1,0,3,2] row_mask:0xf bank_mask:0xf
	s_and_saveexec_b64 s[0:1], s[4:5]
	s_cbranch_execz .LBB0_803
	s_waitcnt lgkmcnt(0)
	v_cvt_pk_bf16_f32 v2, v24, v2
	global_store_dword v[66:67], v2, off offset:2688
.LBB0_803:
	s_or_b64 exec, exec, s[0:1]
	s_waitcnt lgkmcnt(0)
	v_mov_b32_dpp v2, v8 quad_perm:[1,0,3,2] row_mask:0xf bank_mask:0xf
	s_and_saveexec_b64 s[0:1], s[4:5]
	s_cbranch_execz .LBB0_805
	s_waitcnt lgkmcnt(0)
	v_cvt_pk_bf16_f32 v2, v8, v2
	global_store_dword v[66:67], v2, off offset:2752
.LBB0_805:
	s_or_b64 exec, exec, s[0:1]
	s_waitcnt lgkmcnt(0)
	v_mov_b32_dpp v2, v57 quad_perm:[1,0,3,2] row_mask:0xf bank_mask:0xf
	s_and_saveexec_b64 s[0:1], s[4:5]
	s_cbranch_execz .LBB0_807
	s_waitcnt lgkmcnt(0)
	v_cvt_pk_bf16_f32 v2, v57, v2
	global_store_dword v[66:67], v2, off offset:2816
.LBB0_807:
	s_or_b64 exec, exec, s[0:1]
	s_waitcnt lgkmcnt(0)
	v_mov_b32_dpp v2, v41 quad_perm:[1,0,3,2] row_mask:0xf bank_mask:0xf
	s_and_saveexec_b64 s[0:1], s[4:5]
	s_cbranch_execz .LBB0_809
	s_waitcnt lgkmcnt(0)
	v_cvt_pk_bf16_f32 v2, v41, v2
	global_store_dword v[66:67], v2, off offset:2880
.LBB0_809:
	s_or_b64 exec, exec, s[0:1]
	s_waitcnt lgkmcnt(0)
	v_mov_b32_dpp v2, v25 quad_perm:[1,0,3,2] row_mask:0xf bank_mask:0xf
	s_and_saveexec_b64 s[0:1], s[4:5]
	s_cbranch_execz .LBB0_811
	s_waitcnt lgkmcnt(0)
	v_cvt_pk_bf16_f32 v2, v25, v2
	global_store_dword v[66:67], v2, off offset:2944
.LBB0_811:
	s_or_b64 exec, exec, s[0:1]
	s_waitcnt lgkmcnt(0)
	v_mov_b32_dpp v2, v9 quad_perm:[1,0,3,2] row_mask:0xf bank_mask:0xf
	s_and_saveexec_b64 s[0:1], s[4:5]
	s_cbranch_execz .LBB0_813
	s_waitcnt lgkmcnt(0)
	v_cvt_pk_bf16_f32 v2, v9, v2
	global_store_dword v[66:67], v2, off offset:3008
.LBB0_813:
	s_or_b64 exec, exec, s[0:1]
	s_waitcnt lgkmcnt(0)
	v_mov_b32_dpp v2, v58 quad_perm:[1,0,3,2] row_mask:0xf bank_mask:0xf
	s_and_saveexec_b64 s[0:1], s[4:5]
	s_cbranch_execz .LBB0_815
	s_waitcnt lgkmcnt(0)
	v_cvt_pk_bf16_f32 v4, v58, v2
	v_add_co_u32_e32 v2, vcc, 0x1000, v66
	s_nop 1
	v_addc_co_u32_e32 v3, vcc, 0, v67, vcc
	global_store_dword v[2:3], v4, off
.LBB0_815:
	s_or_b64 exec, exec, s[0:1]
	s_waitcnt lgkmcnt(0)
	v_mov_b32_dpp v2, v42 quad_perm:[1,0,3,2] row_mask:0xf bank_mask:0xf
	s_and_saveexec_b64 s[0:1], s[4:5]
	s_cbranch_execz .LBB0_817
	s_waitcnt lgkmcnt(0)
	v_cvt_pk_bf16_f32 v4, v42, v2
	v_add_co_u32_e32 v2, vcc, 0x1000, v66
	s_nop 1
	v_addc_co_u32_e32 v3, vcc, 0, v67, vcc
	global_store_dword v[2:3], v4, off offset:64
.LBB0_817:
	s_or_b64 exec, exec, s[0:1]
	s_waitcnt lgkmcnt(0)
	v_mov_b32_dpp v2, v26 quad_perm:[1,0,3,2] row_mask:0xf bank_mask:0xf
	s_and_saveexec_b64 s[0:1], s[4:5]
	s_cbranch_execz .LBB0_819
	s_waitcnt lgkmcnt(0)
	v_cvt_pk_bf16_f32 v4, v26, v2
	v_add_co_u32_e32 v2, vcc, 0x1000, v66
	s_nop 1
	v_addc_co_u32_e32 v3, vcc, 0, v67, vcc
	global_store_dword v[2:3], v4, off offset:128
.LBB0_819:
	s_or_b64 exec, exec, s[0:1]
	s_waitcnt lgkmcnt(0)
	v_mov_b32_dpp v2, v10 quad_perm:[1,0,3,2] row_mask:0xf bank_mask:0xf
	s_and_saveexec_b64 s[0:1], s[4:5]
	s_cbranch_execz .LBB0_821
	s_waitcnt lgkmcnt(0)
	v_cvt_pk_bf16_f32 v4, v10, v2
	v_add_co_u32_e32 v2, vcc, 0x1000, v66
	s_nop 1
	v_addc_co_u32_e32 v3, vcc, 0, v67, vcc
	global_store_dword v[2:3], v4, off offset:192
; __device__ __forceinline__ int crow(int r, int hi) { return (r & 3) + 8 * (r >> 2) + 4 * hi; }
; template <class TIn, class TOut>
; __device__ __forceinline__ void causal_swa_block(const BlockRef<TIn, TOut>& cur, const BlockRef<TIn, TOut>& nxt, int skv, int W, char* lds, Seam<TIn>& S) {
;     ...
;         for (int r = 0; r < 16; ++r) { const int orow = crow(r, hi);
; #pragma unroll
;             for (int d0 = 0; d0 < 4; ++d0) { const float v = o[d0][r]; const float vn = __shfl_xor(v, 1);
;                 if ((r32 & 1) == 0) __builtin_nontemporal_store(cvtpk(v, vn), (unsigned*)(Pw + (size_t)orow * 128 + d0 * 32 + r32)); } }
.LBB0_821:
	s_or_b64 exec, exec, s[0:1]
	s_waitcnt lgkmcnt(0)
	v_mov_b32_dpp v2, v59 quad_perm:[1,0,3,2] row_mask:0xf bank_mask:0xf
	s_and_saveexec_b64 s[0:1], s[4:5]
	s_cbranch_execz .LBB0_823
	s_waitcnt lgkmcnt(0)
	v_cvt_pk_bf16_f32 v4, v59, v2
	v_add_co_u32_e32 v2, vcc, 0x1000, v66
	s_nop 1
	v_addc_co_u32_e32 v3, vcc, 0, v67, vcc
	global_store_dword v[2:3], v4, off offset:256
.LBB0_823:
	s_or_b64 exec, exec, s[0:1]
	s_waitcnt lgkmcnt(0)
	v_mov_b32_dpp v2, v43 quad_perm:[1,0,3,2] row_mask:0xf bank_mask:0xf
	s_and_saveexec_b64 s[0:1], s[4:5]
	s_cbranch_execz .LBB0_825
	s_waitcnt lgkmcnt(0)
	v_cvt_pk_bf16_f32 v4, v43, v2
	v_add_co_u32_e32 v2, vcc, 0x1000, v66
	s_nop 1
	v_addc_co_u32_e32 v3, vcc, 0, v67, vcc
	global_store_dword v[2:3], v4, off offset:320
.LBB0_825:
	s_or_b64 exec, exec, s[0:1]
	s_waitcnt lgkmcnt(0)
	v_mov_b32_dpp v2, v27 quad_perm:[1,0,3,2] row_mask:0xf bank_mask:0xf
	s_and_saveexec_b64 s[0:1], s[4:5]
	s_cbranch_execz .LBB0_827
	s_waitcnt lgkmcnt(0)
	v_cvt_pk_bf16_f32 v4, v27, v2
	v_add_co_u32_e32 v2, vcc, 0x1000, v66
	s_nop 1
	v_addc_co_u32_e32 v3, vcc, 0, v67, vcc
	global_store_dword v[2:3], v4, off offset:384
.LBB0_827:
	s_or_b64 exec, exec, s[0:1]
	s_waitcnt lgkmcnt(0)
	v_mov_b32_dpp v2, v11 quad_perm:[1,0,3,2] row_mask:0xf bank_mask:0xf
	s_and_saveexec_b64 s[0:1], s[4:5]
	s_cbranch_execz .LBB0_829
	s_waitcnt lgkmcnt(0)
	v_cvt_pk_bf16_f32 v4, v11, v2
	v_add_co_u32_e32 v2, vcc, 0x1000, v66
	s_nop 1
	v_addc_co_u32_e32 v3, vcc, 0, v67, vcc
	global_store_dword v[2:3], v4, off offset:448
.LBB0_829:
	s_or_b64 exec, exec, s[0:1]
	s_waitcnt lgkmcnt(0)
	v_mov_b32_dpp v2, v60 quad_perm:[1,0,3,2] row_mask:0xf bank_mask:0xf
	s_and_saveexec_b64 s[0:1], s[4:5]
	s_cbranch_execz .LBB0_831
	s_waitcnt lgkmcnt(0)
	v_cvt_pk_bf16_f32 v4, v60, v2
	v_add_co_u32_e32 v2, vcc, 0x1000, v66
	s_nop 1
	v_addc_co_u32_e32 v3, vcc, 0, v67, vcc
	global_store_dword v[2:3], v4, off offset:512
.LBB0_831:
	s_or_b64 exec, exec, s[0:1]
	s_waitcnt lgkmcnt(0)
	v_mov_b32_dpp v2, v44 quad_perm:[1,0,3,2] row_mask:0xf bank_mask:0xf
	s_and_saveexec_b64 s[0:1], s[4:5]
	s_cbranch_execz .LBB0_833
	s_waitcnt lgkmcnt(0)
	v_cvt_pk_bf16_f32 v4, v44, v2
	v_add_co_u32_e32 v2, vcc, 0x1000, v66
	s_nop 1
	v_addc_co_u32_e32 v3, vcc, 0, v67, vcc
	global_store_dword v[2:3], v4, off offset:576
.LBB0_833:
	s_or_b64 exec, exec, s[0:1]
	s_waitcnt lgkmcnt(0)
	v_mov_b32_dpp v2, v28 quad_perm:[1,0,3,2] row_mask:0xf bank_mask:0xf
	s_and_saveexec_b64 s[0:1], s[4:5]
	s_cbranch_execz .LBB0_835
	s_waitcnt lgkmcnt(0)
	v_cvt_pk_bf16_f32 v4, v28, v2
	v_add_co_u32_e32 v2, vcc, 0x1000, v66
	s_nop 1
	v_addc_co_u32_e32 v3, vcc, 0, v67, vcc
	global_store_dword v[2:3], v4, off offset:640
.LBB0_835:
	s_or_b64 exec, exec, s[0:1]
	s_waitcnt lgkmcnt(0)
	v_mov_b32_dpp v2, v12 quad_perm:[1,0,3,2] row_mask:0xf bank_mask:0xf
	s_and_saveexec_b64 s[0:1], s[4:5]
	s_cbranch_execz .LBB0_837
	s_waitcnt lgkmcnt(0)
	v_cvt_pk_bf16_f32 v4, v12, v2
	v_add_co_u32_e32 v2, vcc, 0x1000, v66
	s_nop 1
	v_addc_co_u32_e32 v3, vcc, 0, v67, vcc
	global_store_dword v[2:3], v4, off offset:704
.LBB0_837:
	s_or_b64 exec, exec, s[0:1]
	s_waitcnt lgkmcnt(0)
	v_mov_b32_dpp v2, v61 quad_perm:[1,0,3,2] row_mask:0xf bank_mask:0xf
	s_and_saveexec_b64 s[0:1], s[4:5]
	s_cbranch_execz .LBB0_839
	s_waitcnt lgkmcnt(0)
	v_cvt_pk_bf16_f32 v4, v61, v2
	v_add_co_u32_e32 v2, vcc, 0x1000, v66
	s_nop 1
	v_addc_co_u32_e32 v3, vcc, 0, v67, vcc
	global_store_dword v[2:3], v4, off offset:768
.LBB0_839:
	s_or_b64 exec, exec, s[0:1]
	s_waitcnt lgkmcnt(0)
	v_mov_b32_dpp v2, v45 quad_perm:[1,0,3,2] row_mask:0xf bank_mask:0xf
	s_and_saveexec_b64 s[0:1], s[4:5]
	s_cbranch_execz .LBB0_841
	s_waitcnt lgkmcnt(0)
	v_cvt_pk_bf16_f32 v4, v45, v2
	v_add_co_u32_e32 v2, vcc, 0x1000, v66
	s_nop 1
	v_addc_co_u32_e32 v3, vcc, 0, v67, vcc
	global_store_dword v[2:3], v4, off offset:832
.LBB0_841:
	s_or_b64 exec, exec, s[0:1]
	s_waitcnt lgkmcnt(0)
	v_mov_b32_dpp v2, v29 quad_perm:[1,0,3,2] row_mask:0xf bank_mask:0xf
	s_and_saveexec_b64 s[0:1], s[4:5]
	s_cbranch_execz .LBB0_843
	s_waitcnt lgkmcnt(0)
	v_cvt_pk_bf16_f32 v4, v29, v2
	v_add_co_u32_e32 v2, vcc, 0x1000, v66
	s_nop 1
	v_addc_co_u32_e32 v3, vcc, 0, v67, vcc
	global_store_dword v[2:3], v4, off offset:896
.LBB0_843:
	s_or_b64 exec, exec, s[0:1]
	s_waitcnt lgkmcnt(0)
	v_mov_b32_dpp v2, v13 quad_perm:[1,0,3,2] row_mask:0xf bank_mask:0xf
	s_and_saveexec_b64 s[0:1], s[4:5]
	s_cbranch_execz .LBB0_845
	s_waitcnt lgkmcnt(0)
	v_cvt_pk_bf16_f32 v4, v13, v2
	v_add_co_u32_e32 v2, vcc, 0x1000, v66
	s_nop 1
	v_addc_co_u32_e32 v3, vcc, 0, v67, vcc
	global_store_dword v[2:3], v4, off offset:960
.LBB0_845:
	s_or_b64 exec, exec, s[0:1]
	s_waitcnt lgkmcnt(0)
	v_mov_b32_dpp v2, v62 quad_perm:[1,0,3,2] row_mask:0xf bank_mask:0xf
	s_and_saveexec_b64 s[0:1], s[4:5]
	s_cbranch_execz .LBB0_847
	s_waitcnt lgkmcnt(0)
	v_cvt_pk_bf16_f32 v4, v62, v2
	v_add_co_u32_e32 v2, vcc, 0x1000, v66
	s_nop 1
	v_addc_co_u32_e32 v3, vcc, 0, v67, vcc
	global_store_dword v[2:3], v4, off offset:2048
.LBB0_847:
	s_or_b64 exec, exec, s[0:1]
	s_waitcnt lgkmcnt(0)
	v_mov_b32_dpp v2, v46 quad_perm:[1,0,3,2] row_mask:0xf bank_mask:0xf
	s_and_saveexec_b64 s[0:1], s[4:5]
	s_cbranch_execz .LBB0_849
	s_waitcnt lgkmcnt(0)
	v_cvt_pk_bf16_f32 v4, v46, v2
	v_add_co_u32_e32 v2, vcc, 0x1000, v66
	s_nop 1
	v_addc_co_u32_e32 v3, vcc, 0, v67, vcc
	global_store_dword v[2:3], v4, off offset:2112
; __device__ __forceinline__ int crow(int r, int hi) { return (r & 3) + 8 * (r >> 2) + 4 * hi; }
; template <class TIn, class TOut>
; __device__ __forceinline__ void causal_swa_block(const BlockRef<TIn, TOut>& cur, const BlockRef<TIn, TOut>& nxt, int skv, int W, char* lds, Seam<TIn>& S) {
;     ...
;         for (int r = 0; r < 16; ++r) { const int orow = crow(r, hi);
; #pragma unroll
;             for (int d0 = 0; d0 < 4; ++d0) { const float v = o[d0][r]; const float vn = __shfl_xor(v, 1);
;                 if ((r32 & 1) == 0) __builtin_nontemporal_store(cvtpk(v, vn), (unsigned*)(Pw + (size_t)orow * 128 + d0 * 32 + r32)); } }
.LBB0_849:
	s_or_b64 exec, exec, s[0:1]
	s_waitcnt lgkmcnt(0)
	v_mov_b32_dpp v2, v30 quad_perm:[1,0,3,2] row_mask:0xf bank_mask:0xf
	s_and_saveexec_b64 s[0:1], s[4:5]
	s_cbranch_execz .LBB0_851
	s_waitcnt lgkmcnt(0)
	v_cvt_pk_bf16_f32 v4, v30, v2
	v_add_co_u32_e32 v2, vcc, 0x1000, v66
	s_nop 1
	v_addc_co_u32_e32 v3, vcc, 0, v67, vcc
	global_store_dword v[2:3], v4, off offset:2176
.LBB0_851:
	s_or_b64 exec, exec, s[0:1]
	s_waitcnt lgkmcnt(0)
	v_mov_b32_dpp v2, v14 quad_perm:[1,0,3,2] row_mask:0xf bank_mask:0xf
	s_and_saveexec_b64 s[0:1], s[4:5]
	s_cbranch_execz .LBB0_853
	s_waitcnt lgkmcnt(0)
	v_cvt_pk_bf16_f32 v4, v14, v2
	v_add_co_u32_e32 v2, vcc, 0x1000, v66
	s_nop 1
	v_addc_co_u32_e32 v3, vcc, 0, v67, vcc
	global_store_dword v[2:3], v4, off offset:2240
.LBB0_853:
	s_or_b64 exec, exec, s[0:1]
	s_waitcnt lgkmcnt(0)
	v_mov_b32_dpp v2, v63 quad_perm:[1,0,3,2] row_mask:0xf bank_mask:0xf
	s_and_saveexec_b64 s[0:1], s[4:5]
	s_cbranch_execz .LBB0_855
	s_waitcnt lgkmcnt(0)
	v_cvt_pk_bf16_f32 v4, v63, v2
	v_add_co_u32_e32 v2, vcc, 0x1000, v66
	s_nop 1
	v_addc_co_u32_e32 v3, vcc, 0, v67, vcc
	global_store_dword v[2:3], v4, off offset:2304
.LBB0_855:
	s_or_b64 exec, exec, s[0:1]
	s_waitcnt lgkmcnt(0)
	v_mov_b32_dpp v2, v47 quad_perm:[1,0,3,2] row_mask:0xf bank_mask:0xf
	s_and_saveexec_b64 s[0:1], s[4:5]
	s_cbranch_execz .LBB0_857
	s_waitcnt lgkmcnt(0)
	v_cvt_pk_bf16_f32 v4, v47, v2
	v_add_co_u32_e32 v2, vcc, 0x1000, v66
	s_nop 1
	v_addc_co_u32_e32 v3, vcc, 0, v67, vcc
	global_store_dword v[2:3], v4, off offset:2368
.LBB0_857:
	s_or_b64 exec, exec, s[0:1]
	s_waitcnt lgkmcnt(0)
	v_mov_b32_dpp v2, v31 quad_perm:[1,0,3,2] row_mask:0xf bank_mask:0xf
	s_and_saveexec_b64 s[0:1], s[4:5]
	s_cbranch_execz .LBB0_859
	s_waitcnt lgkmcnt(0)
	v_cvt_pk_bf16_f32 v4, v31, v2
	v_add_co_u32_e32 v2, vcc, 0x1000, v66
	s_nop 1
	v_addc_co_u32_e32 v3, vcc, 0, v67, vcc
	global_store_dword v[2:3], v4, off offset:2432
.LBB0_859:
	s_or_b64 exec, exec, s[0:1]
	s_waitcnt lgkmcnt(0)
	v_mov_b32_dpp v2, v15 quad_perm:[1,0,3,2] row_mask:0xf bank_mask:0xf
	s_and_saveexec_b64 s[0:1], s[4:5]
	s_cbranch_execz .LBB0_861
	s_waitcnt lgkmcnt(0)
	v_cvt_pk_bf16_f32 v4, v15, v2
	v_add_co_u32_e32 v2, vcc, 0x1000, v66
	s_nop 1
	v_addc_co_u32_e32 v3, vcc, 0, v67, vcc
	global_store_dword v[2:3], v4, off offset:2496
.LBB0_861:
	s_or_b64 exec, exec, s[0:1]
	s_waitcnt lgkmcnt(0)
	v_mov_b32_dpp v2, v64 quad_perm:[1,0,3,2] row_mask:0xf bank_mask:0xf
	s_and_saveexec_b64 s[0:1], s[4:5]
	s_cbranch_execz .LBB0_863
	s_waitcnt lgkmcnt(0)
	v_cvt_pk_bf16_f32 v4, v64, v2
	v_add_co_u32_e32 v2, vcc, 0x1000, v66
	s_nop 1
	v_addc_co_u32_e32 v3, vcc, 0, v67, vcc
	global_store_dword v[2:3], v4, off offset:2560
.LBB0_863:
	s_or_b64 exec, exec, s[0:1]
	s_waitcnt lgkmcnt(0)
	v_mov_b32_dpp v2, v48 quad_perm:[1,0,3,2] row_mask:0xf bank_mask:0xf
	s_and_saveexec_b64 s[0:1], s[4:5]
	s_cbranch_execz .LBB0_865
	s_waitcnt lgkmcnt(0)
	v_cvt_pk_bf16_f32 v4, v48, v2
	v_add_co_u32_e32 v2, vcc, 0x1000, v66
	s_nop 1
	v_addc_co_u32_e32 v3, vcc, 0, v67, vcc
	global_store_dword v[2:3], v4, off offset:2624
.LBB0_865:
	s_or_b64 exec, exec, s[0:1]
	s_waitcnt lgkmcnt(0)
	v_mov_b32_dpp v2, v32 quad_perm:[1,0,3,2] row_mask:0xf bank_mask:0xf
	s_and_saveexec_b64 s[0:1], s[4:5]
	s_cbranch_execz .LBB0_867
	s_waitcnt lgkmcnt(0)
	v_cvt_pk_bf16_f32 v4, v32, v2
	v_add_co_u32_e32 v2, vcc, 0x1000, v66
	s_nop 1
	v_addc_co_u32_e32 v3, vcc, 0, v67, vcc
	global_store_dword v[2:3], v4, off offset:2688
.LBB0_867:
	s_or_b64 exec, exec, s[0:1]
	s_waitcnt lgkmcnt(0)
	v_mov_b32_dpp v2, v16 quad_perm:[1,0,3,2] row_mask:0xf bank_mask:0xf
	s_and_saveexec_b64 s[0:1], s[4:5]
	s_cbranch_execz .LBB0_869
	s_waitcnt lgkmcnt(0)
	v_cvt_pk_bf16_f32 v4, v16, v2
	v_add_co_u32_e32 v2, vcc, 0x1000, v66
	s_nop 1
	v_addc_co_u32_e32 v3, vcc, 0, v67, vcc
	global_store_dword v[2:3], v4, off offset:2752
.LBB0_869:
	s_or_b64 exec, exec, s[0:1]
	s_waitcnt lgkmcnt(0)
	v_mov_b32_dpp v2, v65 quad_perm:[1,0,3,2] row_mask:0xf bank_mask:0xf
	s_and_saveexec_b64 s[0:1], s[4:5]
	s_cbranch_execz .LBB0_871
	s_waitcnt lgkmcnt(0)
	v_cvt_pk_bf16_f32 v4, v65, v2
	v_add_co_u32_e32 v2, vcc, 0x1000, v66
	s_nop 1
	v_addc_co_u32_e32 v3, vcc, 0, v67, vcc
	global_store_dword v[2:3], v4, off offset:2816
.LBB0_871:
	s_or_b64 exec, exec, s[0:1]
	s_waitcnt lgkmcnt(0)
	v_mov_b32_dpp v2, v49 quad_perm:[1,0,3,2] row_mask:0xf bank_mask:0xf
	s_and_saveexec_b64 s[0:1], s[4:5]
	s_cbranch_execz .LBB0_873
	s_waitcnt lgkmcnt(0)
	v_cvt_pk_bf16_f32 v4, v49, v2
	v_add_co_u32_e32 v2, vcc, 0x1000, v66
	s_nop 1
	v_addc_co_u32_e32 v3, vcc, 0, v67, vcc
	global_store_dword v[2:3], v4, off offset:2880
.LBB0_873:
	s_or_b64 exec, exec, s[0:1]
	s_waitcnt lgkmcnt(0)
	v_mov_b32_dpp v2, v33 quad_perm:[1,0,3,2] row_mask:0xf bank_mask:0xf
	s_and_saveexec_b64 s[0:1], s[4:5]
	s_cbranch_execz .LBB0_875
	s_waitcnt lgkmcnt(0)
	v_cvt_pk_bf16_f32 v4, v33, v2
	v_add_co_u32_e32 v2, vcc, 0x1000, v66
	s_nop 1
	v_addc_co_u32_e32 v3, vcc, 0, v67, vcc
	global_store_dword v[2:3], v4, off offset:2944
.LBB0_875:
	s_or_b64 exec, exec, s[0:1]
	s_waitcnt lgkmcnt(0)
	v_mov_b32_dpp v2, v17 quad_perm:[1,0,3,2] row_mask:0xf bank_mask:0xf
	s_and_saveexec_b64 s[0:1], s[4:5]
	s_cbranch_execz .LBB0_877
	s_waitcnt lgkmcnt(0)
	v_cvt_pk_bf16_f32 v4, v17, v2
	v_add_co_u32_e32 v2, vcc, 0x1000, v66
	s_nop 1
	v_addc_co_u32_e32 v3, vcc, 0, v67, vcc
	global_store_dword v[2:3], v4, off offset:3008
